# phase 3 in four (query-half,row-tile) chunks: each chunk's 4 stores issue under the next chunk's MFMAs, only 4 stores left exposed
# baseline (speedup 1.0000x reference)
.LBB1_4:
	s_or_b64 exec, exec, s[4:5]
	v_lshl_or_b32 v4, v27, 1, v96
	v_lshl_or_b32 v3, v4, 7, v3
	v_or_b32_e32 v5, 0x23600, v3
	v_or_b32_e32 v3, 0x23640, v3
	s_waitcnt lgkmcnt(0)
	s_barrier
	ds_read_b32 v5, v5
	ds_read_b32 v3, v3
	v_mad_u32_u24 v4, v4, s7, v13
	v_lshl_add_u32 v4, v119, 4, v4
	v_or_b32_e32 v6, 0x20000, v4
	ds_read_b128 v[16:19], v6
	s_waitcnt lgkmcnt(1)
	v_add_f32_e32 v3, v5, v3
	v_add_u32_e32 v5, 0x20020, v4
	v_add_u32_e32 v6, 0x20040, v4
	ds_read_b128 v[112:115], v5
	ds_read_b128 v[108:111], v6
	v_add_u32_e32 v5, 0x20060, v4
	v_add_u32_e32 v6, 0x20080, v4
	v_lshlrev_b32_e32 v7, 1, v101
	ds_read_b128 v[104:107], v5
	ds_read_b128 v[96:99], v6
	v_lshrrev_b32_e32 v5, 2, v100
	v_or_b32_e32 v6, v28, v125
	v_and_b32_e32 v7, 2, v7
	v_bfe_u32 v8, v0, 1, 1
	v_and_b32_e32 v164, 8, v121
	v_bfe_i32 v9, v0, 7, 1
	v_or3_b32 v8, v8, v7, v164
	v_and_b32_e32 v0, 12, v0
	v_add_lshl_u32 v10, v6, v5, 8
	v_or_b32_e32 v5, v6, v5
	v_and_b32_e32 v9, 0xc000, v9
	v_lshlrev_b32_e32 v12, 8, v5
	v_bitop3_b32 v5, v0, v8, v124 bitop3:0x36
	v_lshl_or_b32 v13, v5, 4, v9
	v_bitop3_b32 v6, v0, v8, v2 bitop3:0x36
	v_or_b32_e32 v15, 0x1000, v12
	v_lshl_or_b32 v14, v6, 4, v9
	v_add_u32_e32 v7, v13, v15
	v_or_b32_e32 v24, 0x1400, v12
	v_or_b32_e32 v20, v7, v1
	v_add_u32_e32 v7, v14, v24
	v_add_u32_e32 v25, 0x2000, v10
	v_add_u32_e32 v5, v13, v12
	v_add_u32_e32 v6, v14, v12
	v_or_b32_e32 v22, v7, v1
	v_add_u32_e32 v7, v13, v25
	v_add_u32_e32 v150, 0x3000, v10
	v_or_b32_e32 v8, 4, v8
	v_add_u32_e32 v4, 0x200a0, v4
	v_or_b32_e32 v5, v5, v1
	v_or_b32_e32 v6, v6, v1
	v_or_b32_e32 v27, v7, v1
	v_add_u32_e32 v31, v13, v150
	v_add_u32_e32 v151, 0x3400, v10
	v_bitop3_b32 v124, v0, v8, v124 bitop3:0x36
	v_bitop3_b32 v0, v0, v8, v2 bitop3:0x36
	ds_read_b128 v[100:103], v4
	ds_read_b64_tr_b16 v[4:5], v5
	ds_read_b64_tr_b16 v[6:7], v6 offset:1024
	ds_read_b64_tr_b16 v[20:21], v20
	ds_read_b64_tr_b16 v[22:23], v22
	ds_read_b64_tr_b16 v[28:29], v27
	v_add_u32_e32 v27, 0x2400, v10
	v_or_b32_e32 v128, v31, v1
	v_add_u32_e32 v31, v14, v151
	v_add_u32_e32 v152, 0x4000, v10
	v_add_u32_e32 v158, 0x4400, v10
	v_lshl_or_b32 v124, v124, 4, v9
	v_lshl_or_b32 v0, v0, 4, v9
	v_add_u32_e32 v11, 0x5000, v10
	v_add_u32_e32 v30, v14, v27
	v_or_b32_e32 v130, v31, v1
	v_add_u32_e32 v31, v13, v152
	v_add_u32_e32 v134, v14, v158
	v_add_u32_e32 v10, 0x5400, v10
	v_add_u32_e32 v135, v124, v12
	v_add_u32_e32 v2, v0, v12
	v_add_u32_e32 v8, v124, v15
	v_or_b32_e32 v30, v30, v1
	v_or_b32_e32 v132, v31, v1
	v_or_b32_e32 v134, v134, v1
	v_add_u32_e32 v13, v13, v11
	v_add_u32_e32 v14, v14, v10
	v_or_b32_e32 v140, v135, v1
	v_or_b32_e32 v2, v2, v1
	v_or_b32_e32 v8, v8, v1
	v_add_u32_e32 v9, v0, v24
	v_add_u32_e32 v12, v124, v25
	ds_read_b64_tr_b16 v[30:31], v30
	ds_read_b64_tr_b16 v[128:129], v128
	ds_read_b64_tr_b16 v[130:131], v130
	ds_read_b64_tr_b16 v[132:133], v132
	v_or_b32_e32 v13, v13, v1
	v_or_b32_e32 v14, v14, v1
	ds_read_b64_tr_b16 v[134:135], v134
	ds_read_b64_tr_b16 v[136:137], v13
	ds_read_b64_tr_b16 v[138:139], v14
	ds_read_b64_tr_b16 v[140:141], v140
	v_or_b32_e32 v9, v9, v1
	v_or_b32_e32 v12, v12, v1
	ds_read_b64_tr_b16 v[142:143], v2 offset:1024
	ds_read_b64_tr_b16 v[144:145], v8
	ds_read_b64_tr_b16 v[146:147], v9
	ds_read_b64_tr_b16 v[148:149], v12
	v_add_u32_e32 v2, v0, v27
	v_add_u32_e32 v8, v124, v150
	v_or_b32_e32 v2, v2, v1
	v_or_b32_e32 v8, v8, v1
	v_add_u32_e32 v9, v0, v151
	v_add_u32_e32 v12, v124, v152
	v_or_b32_e32 v9, v9, v1
	v_or_b32_e32 v12, v12, v1
	ds_read_b64_tr_b16 v[150:151], v2
	ds_read_b64_tr_b16 v[152:153], v8
	ds_read_b64_tr_b16 v[154:155], v9
	ds_read_b64_tr_b16 v[156:157], v12
	v_add_u32_e32 v2, v0, v158
	v_add_u32_e32 v8, v124, v11
	v_add_u32_e32 v0, v0, v10
	v_or_b32_e32 v2, v2, v1
	v_or_b32_e32 v8, v8, v1
	v_or_b32_e32 v0, v0, v1
	v_div_scale_f32 v1, s[8:9], v3, v3, 1.0
	v_rcp_f32_e32 v9, v1
	ds_read_b64_tr_b16 v[158:159], v2
	ds_read_b64_tr_b16 v[160:161], v8
	ds_read_b64_tr_b16 v[162:163], v0
	s_mov_b32 s4, 0xc000
	s_movk_i32 s5, 0x4000
	v_fma_f32 v0, -v1, v9, 1.0
	v_fmac_f32_e32 v9, v0, v9
	v_div_scale_f32 v0, vcc, 1.0, v3, 1.0
	v_mul_f32_e32 v2, v0, v9
	v_fma_f32 v8, -v1, v2, v0
	v_fmac_f32_e32 v2, v8, v9
	v_fma_f32 v0, -v1, v2, v0
	v_div_fmas_f32 v0, v0, v9, v2
	v_div_fixup_f32 v124, v0, v3, 1.0
	s_waitcnt lgkmcnt(14)
	v_mfma_f32_32x32x16_f16 v[0:15], v[4:7], v[16:19], 0
	s_mov_b32 s7, 0x18000
	v_lshlrev_b32_e32 v172, 2, v126
	v_mov_b32_e32 v173, 0
	v_mfma_f32_32x32x16_f16 v[0:15], v[20:23], v[112:115], v[0:15]
	v_or_b32_e32 v20, v26, v116
	v_and_b32_e32 v21, 0x4000, v118
	v_lshl_or_b32 v20, v20, 8, v21
	v_bitop3_b32 v118, v121, v120, 8 bitop3:0x6c
	v_or3_b32 v121, v20, v125, s7
	v_mfma_f32_32x32x16_f16 v[0:15], v[28:31], v[108:111], v[0:15]
	v_mfma_f32_32x32x16_f16 v[0:15], v[128:131], v[104:107], v[0:15]
	v_mfma_f32_32x32x16_f16 v[0:15], v[132:135], v[96:99], v[0:15]
	s_waitcnt lgkmcnt(12)
	v_mfma_f32_32x32x16_f16 v[0:15], v[136:139], v[100:103], v[0:15]
	s_nop 11
	v_fma_mixlo_f16 v20, v124, v0, 0
	v_mov_b32_e32 v0, v1
	v_mov_b32_e32 v1, v2
	v_pk_mul_f32 v[0:1], v[124:125], v[0:1] op_sel_hi:[0,1]
	v_cvt_pk_f16_f32 v1, v0, v1
	v_pack_b32_f16 v0, v20, v1
	s_waitcnt lgkmcnt(10)
	v_mfma_f32_32x32x16_f16 v[16:31], v[140:143], v[16:19], 0
	v_fma_mixlo_f16 v2, v124, v3, 0
	v_alignbit_b32 v1, v2, v1, 16
	v_lshl_or_b32 v2, v118, 4, v121
	ds_write_b64 v2, v[0:1]
	v_mov_b32_e32 v0, v5
	v_mov_b32_e32 v1, v6
	v_pk_mul_f32 v[0:1], v[124:125], v[0:1] op_sel_hi:[0,1]
	s_waitcnt lgkmcnt(9)
	v_mfma_f32_32x32x16_f16 v[16:31], v[144:147], v[112:115], v[16:31]
	v_fma_mixlo_f16 v2, v124, v4, 0
	v_cvt_pk_f16_f32 v1, v0, v1
	v_pack_b32_f16 v0, v2, v1
	v_fma_mixlo_f16 v2, v124, v7, 0
	v_alignbit_b32 v1, v2, v1, 16
	v_bitop3_b32 v2, v164, v120, 1 bitop3:0x36
	v_lshl_or_b32 v2, v2, 4, v121
	s_waitcnt lgkmcnt(7)
	v_mfma_f32_32x32x16_f16 v[16:31], v[148:151], v[108:111], v[16:31]
	ds_write_b64 v2, v[0:1]
	v_mov_b32_e32 v0, v9
	v_mov_b32_e32 v1, v10
	v_mul_f32_e64 v0, v124, v0
	v_mul_f32_e64 v1, v124, v1
	v_fma_mixlo_f16 v2, v124, v8, 0
	v_cvt_pk_f16_f32 v1, v0, v1
	v_pack_b32_f16 v0, v2, v1
	s_waitcnt lgkmcnt(6)
	v_mfma_f32_32x32x16_f16 v[16:31], v[152:155], v[104:107], v[16:31]
	v_fma_mixlo_f16 v2, v124, v11, 0
	v_alignbit_b32 v1, v2, v1, 16
	v_bitop3_b32 v2, v164, v120, 2 bitop3:0x36
	v_lshl_or_b32 v2, v2, 4, v121
	ds_write_b64 v2, v[0:1]
	v_mov_b32_e32 v0, v13
	v_mov_b32_e32 v1, v14
	s_waitcnt lgkmcnt(5)
	v_mfma_f32_32x32x16_f16 v[16:31], v[156:159], v[96:99], v[16:31]
	v_mul_f32_e64 v0, v124, v0
	v_mul_f32_e64 v1, v124, v1
	v_fma_mixlo_f16 v2, v124, v12, 0
	v_cvt_pk_f16_f32 v1, v0, v1
	v_pack_b32_f16 v0, v2, v1
	v_fma_mixlo_f16 v2, v124, v15, 0
	v_alignbit_b32 v1, v2, v1, 16
	v_bitop3_b32 v2, v164, v120, 3 bitop3:0x36
	s_waitcnt lgkmcnt(3)
	v_mfma_f32_32x32x16_f16 v[16:31], v[160:163], v[100:103], v[16:31]
	v_lshl_or_b32 v2, v2, 4, v121
	ds_write_b64 v2, v[0:1]
	s_nop 9
	v_mov_b32_e32 v0, v17
	v_mov_b32_e32 v1, v18
	v_pk_mul_f32 v[0:1], v[124:125], v[0:1] op_sel_hi:[0,1]
	v_fma_mixlo_f16 v2, v124, v16, 0
	v_cvt_pk_f16_f32 v1, v0, v1
	v_pack_b32_f16 v0, v2, v1
	v_fma_mixlo_f16 v2, v124, v19, 0
	v_alignbit_b32 v1, v2, v1, 16
	v_bitop3_b32 v2, v164, v120, 4 bitop3:0x36
	v_lshl_or_b32 v2, v2, 4, v121
	ds_write_b64 v2, v[0:1]
	v_mov_b32_e32 v0, v21
	v_mov_b32_e32 v1, v22
	v_pk_mul_f32 v[0:1], v[124:125], v[0:1] op_sel_hi:[0,1]
	v_fma_mixlo_f16 v2, v124, v20, 0
	v_cvt_pk_f16_f32 v1, v0, v1
	v_pack_b32_f16 v0, v2, v1
	v_fma_mixlo_f16 v2, v124, v23, 0
	v_alignbit_b32 v1, v2, v1, 16
	v_bitop3_b32 v2, v164, v120, 5 bitop3:0x36
	v_lshl_or_b32 v2, v2, 4, v121
	ds_write_b64 v2, v[0:1]
	v_mov_b32_e32 v0, v25
	v_mov_b32_e32 v1, v26
	v_pk_mul_f32 v[0:1], v[124:125], v[0:1] op_sel_hi:[0,1]
	v_fma_mixlo_f16 v2, v124, v24, 0
	v_cvt_pk_f16_f32 v1, v0, v1
	v_pack_b32_f16 v0, v2, v1
	v_fma_mixlo_f16 v2, v124, v27, 0
	v_alignbit_b32 v1, v2, v1, 16
	v_bitop3_b32 v2, v164, v120, 6 bitop3:0x36
	v_lshl_or_b32 v2, v2, 4, v121
	ds_write_b64 v2, v[0:1]
	v_mov_b32_e32 v0, v29
	v_mov_b32_e32 v1, v30
	v_pk_mul_f32 v[0:1], v[124:125], v[0:1] op_sel_hi:[0,1]
	v_fma_mixlo_f16 v2, v124, v28, 0
	v_cvt_pk_f16_f32 v1, v0, v1
	v_pack_b32_f16 v0, v2, v1
	v_fma_mixlo_f16 v2, v124, v31, 0
	v_alignbit_b32 v1, v2, v1, 16
	v_bitop3_b32 v2, v164, v120, 7 bitop3:0x36
	v_lshl_or_b32 v2, v2, 4, v121
	ds_write_b64 v2, v[0:1]
	v_lshl_add_u64 v[0:1], s[0:1], 0, v[172:173]
	v_lshlrev_b32_e32 v172, 2, v127
	v_lshl_add_u64 v[0:1], v[0:1], 0, v[172:173]
	s_waitcnt lgkmcnt(0)
	s_barrier
	v_and_b32_e32 v245, 15, v116
	v_lshrrev_b32_e32 v246, 4, v116
	v_lshl_or_b32 v246, v119, 1, v246
	v_lshrrev_b32_e32 v250, 5, v126
	v_and_b32_e32 v250, 7, v250
	v_and_b32_e32 v247, 1, v246
	v_lshrrev_b32_e32 v248, 1, v246
	v_xor_b32_e32 v248, v248, v247
	v_lshl_or_b32 v247, v247, 1, v248
	v_and_b32_e32 v248, 3, v245
	v_lshrrev_b32_e32 v249, 2, v245
	v_lshl_or_b32 v248, v248, 2, v249
	v_xor_b32_e32 v247, v247, v248
	v_lshlrev_b32_e32 v240, 8, v245
	v_lshl_or_b32 v240, v247, 4, v240
	v_add_u32_e32 v240, 0x18000, v240
	v_xor_b32_e32 v241, 64, v240
	v_xor_b32_e32 v242, 0x80, v240
	v_xor_b32_e32 v243, 0xc0, v240
	v_lshlrev_b32_e32 v249, 7, v250
	v_lshl_or_b32 v249, v246, 4, v249
	v_and_b32_e32 v249, 0x3f0, v249
	global_load_dwordx4 v[96:99], v249, s[34:35]
	global_load_dwordx4 v[100:103], v249, s[34:35] offset:64
	v_lshlrev_b32_e32 v244, 19, v250
	v_lshl_or_b32 v244, v246, 16, v244
	v_lshl_or_b32 v244, v245, 3, v244
	v_and_b32_e32 v244, 0x3fff78, v244
	s_lshl_b64 s[22:23], s[2:3], 22
	s_add_u32 s22, s22, s30
	s_addc_u32 s23, s23, s31
	s_lshl_b32 s24, s14, 3
	s_add_u32 s22, s22, s24
	s_addc_u32 s23, s23, 0
	ds_read_b128 v[112:115], v240
	ds_read_b128 v[144:147], v240 offset:8192
	ds_read_b128 v[116:119], v241
	ds_read_b128 v[148:151], v241 offset:8192
	ds_read_b128 v[120:123], v242
	ds_read_b128 v[152:155], v242 offset:8192
	ds_read_b128 v[124:127], v243
	ds_read_b128 v[156:159], v243 offset:8192
	ds_read_b128 v[128:131], v240 offset:16384
	ds_read_b128 v[160:163], v240 offset:24576
	ds_read_b128 v[132:135], v241 offset:16384
	ds_read_b128 v[164:167], v241 offset:24576
	ds_read_b128 v[136:139], v242 offset:16384
	ds_read_b128 v[168:171], v242 offset:24576
	ds_read_b128 v[140:143], v243 offset:16384
	ds_read_b128 v[172:175], v243 offset:24576
	s_waitcnt vmcnt(2)
	s_waitcnt lgkmcnt(14)
	v_mfma_f32_16x16x32_f16 v[0:3], v[36:39], v[112:115], 0
	v_mfma_f32_16x16x32_f16 v[4:7], v[36:39], v[144:147], 0
	s_waitcnt lgkmcnt(12)
	v_mfma_f32_16x16x32_f16 v[0:3], v[32:35], v[116:119], v[0:3]
	v_mfma_f32_16x16x32_f16 v[4:7], v[32:35], v[148:151], v[4:7]
	s_waitcnt lgkmcnt(10)
	v_mfma_f32_16x16x32_f16 v[0:3], v[64:67], v[120:123], v[0:3]
	v_mfma_f32_16x16x32_f16 v[4:7], v[64:67], v[152:155], v[4:7]
	s_waitcnt lgkmcnt(8)
	v_mfma_f32_16x16x32_f16 v[0:3], v[48:51], v[124:127], v[0:3]
	v_mfma_f32_16x16x32_f16 v[4:7], v[48:51], v[156:159], v[4:7]
	s_waitcnt lgkmcnt(6)
	v_mfma_f32_16x16x32_f16 v[0:3], v[92:95], v[128:131], v[0:3]
	v_mfma_f32_16x16x32_f16 v[4:7], v[92:95], v[160:163], v[4:7]
	s_waitcnt lgkmcnt(4)
	v_mfma_f32_16x16x32_f16 v[0:3], v[84:87], v[132:135], v[0:3]
	v_mfma_f32_16x16x32_f16 v[4:7], v[84:87], v[164:167], v[4:7]
	s_waitcnt lgkmcnt(2)
	v_mfma_f32_16x16x32_f16 v[0:3], v[80:83], v[136:139], v[0:3]
	v_mfma_f32_16x16x32_f16 v[4:7], v[80:83], v[168:171], v[4:7]
	s_waitcnt lgkmcnt(0)
	v_mfma_f32_16x16x32_f16 v[0:3], v[88:91], v[140:143], v[0:3]
	v_mfma_f32_16x16x32_f16 v[4:7], v[88:91], v[172:175], v[4:7]
	ds_read_b128 v[176:179], v240 offset:4096
	ds_read_b128 v[208:211], v240 offset:12288
	ds_read_b128 v[180:183], v241 offset:4096
	ds_read_b128 v[212:215], v241 offset:12288
	ds_read_b128 v[184:187], v242 offset:4096
	ds_read_b128 v[216:219], v242 offset:12288
	ds_read_b128 v[188:191], v243 offset:4096
	ds_read_b128 v[220:223], v243 offset:12288
	ds_read_b128 v[192:195], v240 offset:20480
	ds_read_b128 v[224:227], v240 offset:28672
	ds_read_b128 v[196:199], v241 offset:20480
	ds_read_b128 v[228:231], v241 offset:28672
	ds_read_b128 v[200:203], v242 offset:20480
	ds_read_b128 v[232:235], v242 offset:28672
	ds_read_b128 v[204:207], v243 offset:20480
	ds_read_b128 v[236:239], v243 offset:28672
	s_waitcnt vmcnt(0)
	v_mfma_f32_16x16x32_f16 v[8:11], v[76:79], v[112:115], 0
	v_mfma_f32_16x16x32_f16 v[12:15], v[76:79], v[144:147], 0
	v_mfma_f32_16x16x32_f16 v[8:11], v[72:75], v[116:119], v[8:11]
	v_mfma_f32_16x16x32_f16 v[12:15], v[72:75], v[148:151], v[12:15]
	s_nop 3
	s_add_u32 s26, s22, 0x0
	s_addc_u32 s27, s23, 0
	v_add_f32_e32 v104, v0, v96
	v_add_f32_e32 v105, v4, v96
	global_store_dwordx2 v244, v[104:105], s[26:27] nt
	v_mfma_f32_16x16x32_f16 v[8:11], v[68:71], v[120:123], v[8:11]
	v_mfma_f32_16x16x32_f16 v[12:15], v[68:71], v[152:155], v[12:15]
	v_mfma_f32_16x16x32_f16 v[8:11], v[52:55], v[124:127], v[8:11]
	v_mfma_f32_16x16x32_f16 v[12:15], v[52:55], v[156:159], v[12:15]
	s_add_u32 s26, s22, 0x4000
	s_addc_u32 s27, s23, 0
	v_add_f32_e32 v106, v1, v97
	v_add_f32_e32 v107, v5, v97
	global_store_dwordx2 v244, v[106:107], s[26:27] nt
	v_mfma_f32_16x16x32_f16 v[8:11], v[60:63], v[128:131], v[8:11]
	v_mfma_f32_16x16x32_f16 v[12:15], v[60:63], v[160:163], v[12:15]
	v_mfma_f32_16x16x32_f16 v[8:11], v[56:59], v[132:135], v[8:11]
	v_mfma_f32_16x16x32_f16 v[12:15], v[56:59], v[164:167], v[12:15]
	s_add_u32 s26, s22, 0x8000
	s_addc_u32 s27, s23, 0
	v_add_f32_e32 v108, v2, v98
	v_add_f32_e32 v109, v6, v98
	global_store_dwordx2 v244, v[108:109], s[26:27] nt
	v_mfma_f32_16x16x32_f16 v[8:11], v[44:47], v[136:139], v[8:11]
	v_mfma_f32_16x16x32_f16 v[12:15], v[44:47], v[168:171], v[12:15]
	v_mfma_f32_16x16x32_f16 v[8:11], v[40:43], v[140:143], v[8:11]
	v_mfma_f32_16x16x32_f16 v[12:15], v[40:43], v[172:175], v[12:15]
	s_add_u32 s26, s22, 0xc000
	s_addc_u32 s27, s23, 0
	v_add_f32_e32 v110, v3, v99
	v_add_f32_e32 v111, v7, v99
	global_store_dwordx2 v244, v[110:111], s[26:27] nt
	s_waitcnt lgkmcnt(14)
	v_mfma_f32_16x16x32_f16 v[16:19], v[36:39], v[176:179], 0
	v_mfma_f32_16x16x32_f16 v[20:23], v[36:39], v[208:211], 0
	s_waitcnt lgkmcnt(12)
	v_mfma_f32_16x16x32_f16 v[16:19], v[32:35], v[180:183], v[16:19]
	v_mfma_f32_16x16x32_f16 v[20:23], v[32:35], v[212:215], v[20:23]
	s_nop 3
	s_add_u32 s26, s22, 0x40000
	s_addc_u32 s27, s23, 0
	v_add_f32_e32 v104, v8, v100
	v_add_f32_e32 v105, v12, v100
	global_store_dwordx2 v244, v[104:105], s[26:27] nt
	s_waitcnt lgkmcnt(10)
	v_mfma_f32_16x16x32_f16 v[16:19], v[64:67], v[184:187], v[16:19]
	v_mfma_f32_16x16x32_f16 v[20:23], v[64:67], v[216:219], v[20:23]
	s_waitcnt lgkmcnt(8)
	v_mfma_f32_16x16x32_f16 v[16:19], v[48:51], v[188:191], v[16:19]
	v_mfma_f32_16x16x32_f16 v[20:23], v[48:51], v[220:223], v[20:23]
	s_add_u32 s26, s22, 0x44000
	s_addc_u32 s27, s23, 0
	v_add_f32_e32 v106, v9, v101
	v_add_f32_e32 v107, v13, v101
	global_store_dwordx2 v244, v[106:107], s[26:27] nt
	s_waitcnt lgkmcnt(6)
	v_mfma_f32_16x16x32_f16 v[16:19], v[92:95], v[192:195], v[16:19]
	v_mfma_f32_16x16x32_f16 v[20:23], v[92:95], v[224:227], v[20:23]
	s_waitcnt lgkmcnt(4)
	v_mfma_f32_16x16x32_f16 v[16:19], v[84:87], v[196:199], v[16:19]
	v_mfma_f32_16x16x32_f16 v[20:23], v[84:87], v[228:231], v[20:23]
	s_add_u32 s26, s22, 0x48000
	s_addc_u32 s27, s23, 0
	v_add_f32_e32 v108, v10, v102
	v_add_f32_e32 v109, v14, v102
	global_store_dwordx2 v244, v[108:109], s[26:27] nt
	s_waitcnt lgkmcnt(2)
	v_mfma_f32_16x16x32_f16 v[16:19], v[80:83], v[200:203], v[16:19]
	v_mfma_f32_16x16x32_f16 v[20:23], v[80:83], v[232:235], v[20:23]
	s_waitcnt lgkmcnt(0)
	v_mfma_f32_16x16x32_f16 v[16:19], v[88:91], v[204:207], v[16:19]
	v_mfma_f32_16x16x32_f16 v[20:23], v[88:91], v[236:239], v[20:23]
	s_add_u32 s26, s22, 0x4c000
	s_addc_u32 s27, s23, 0
	v_add_f32_e32 v110, v11, v103
	v_add_f32_e32 v111, v15, v103
	global_store_dwordx2 v244, v[110:111], s[26:27] nt
	v_mfma_f32_16x16x32_f16 v[24:27], v[76:79], v[176:179], 0
	v_mfma_f32_16x16x32_f16 v[28:31], v[76:79], v[208:211], 0
	v_mfma_f32_16x16x32_f16 v[24:27], v[72:75], v[180:183], v[24:27]
	v_mfma_f32_16x16x32_f16 v[28:31], v[72:75], v[212:215], v[28:31]
	s_nop 3
	s_add_u32 s26, s22, 0x0
	s_addc_u32 s27, s23, 0
	v_add_f32_e32 v104, v16, v96
	v_add_f32_e32 v105, v20, v96
	global_store_dwordx2 v244, v[104:105], s[26:27] offset:128 nt
	v_mfma_f32_16x16x32_f16 v[24:27], v[68:71], v[184:187], v[24:27]
	v_mfma_f32_16x16x32_f16 v[28:31], v[68:71], v[216:219], v[28:31]
	v_mfma_f32_16x16x32_f16 v[24:27], v[52:55], v[188:191], v[24:27]
	v_mfma_f32_16x16x32_f16 v[28:31], v[52:55], v[220:223], v[28:31]
	s_add_u32 s26, s22, 0x4000
	s_addc_u32 s27, s23, 0
	v_add_f32_e32 v106, v17, v97
	v_add_f32_e32 v107, v21, v97
	global_store_dwordx2 v244, v[106:107], s[26:27] offset:128 nt
	v_mfma_f32_16x16x32_f16 v[24:27], v[60:63], v[192:195], v[24:27]
	v_mfma_f32_16x16x32_f16 v[28:31], v[60:63], v[224:227], v[28:31]
	v_mfma_f32_16x16x32_f16 v[24:27], v[56:59], v[196:199], v[24:27]
	v_mfma_f32_16x16x32_f16 v[28:31], v[56:59], v[228:231], v[28:31]
	s_add_u32 s26, s22, 0x8000
	s_addc_u32 s27, s23, 0
	v_add_f32_e32 v108, v18, v98
	v_add_f32_e32 v109, v22, v98
	global_store_dwordx2 v244, v[108:109], s[26:27] offset:128 nt
	v_mfma_f32_16x16x32_f16 v[24:27], v[44:47], v[200:203], v[24:27]
	v_mfma_f32_16x16x32_f16 v[28:31], v[44:47], v[232:235], v[28:31]
	v_mfma_f32_16x16x32_f16 v[24:27], v[40:43], v[204:207], v[24:27]
	v_mfma_f32_16x16x32_f16 v[28:31], v[40:43], v[236:239], v[28:31]
	s_add_u32 s26, s22, 0xc000
	s_addc_u32 s27, s23, 0
	v_add_f32_e32 v110, v19, v99
	v_add_f32_e32 v111, v23, v99
	global_store_dwordx2 v244, v[110:111], s[26:27] offset:128 nt
	s_nop 7
	s_nop 1
	s_add_u32 s26, s22, 0x40000
	s_addc_u32 s27, s23, 0
	v_add_f32_e32 v104, v24, v100
	v_add_f32_e32 v105, v28, v100
	global_store_dwordx2 v244, v[104:105], s[26:27] offset:128 nt
	s_add_u32 s26, s22, 0x44000
	s_addc_u32 s27, s23, 0
	v_add_f32_e32 v106, v25, v101
	v_add_f32_e32 v107, v29, v101
	global_store_dwordx2 v244, v[106:107], s[26:27] offset:128 nt
	s_add_u32 s26, s22, 0x48000
	s_addc_u32 s27, s23, 0
	v_add_f32_e32 v108, v26, v102
	v_add_f32_e32 v109, v30, v102
	global_store_dwordx2 v244, v[108:109], s[26:27] offset:128 nt
	s_add_u32 s26, s22, 0x4c000
	s_addc_u32 s27, s23, 0
	v_add_f32_e32 v110, v27, v103
	v_add_f32_e32 v111, v31, v103
	global_store_dwordx2 v244, v[110:111], s[26:27] offset:128 nt
	s_endpgm
